# speedup vs baseline: 1.0129x; 1.0129x over previous
_Z13logits_kernelPKDv8_DF16bS1_PKfS3_PDv2_fS5_Pf:
	s_load_dwordx4 s[4:7], s[0:1], 0x0
	s_load_dwordx4 s[12:15], s[0:1], 0x10
	s_load_dwordx4 s[24:27], s[0:1], 0x20
	s_load_dwordx2 s[28:29], s[0:1], 0x30
	s_lshl_b32 s3, s2, 1
	s_and_b32 s3, s3, 14
	s_ashr_i32 s8, s2, 7
	s_bfe_u32 s10, s2, 0x40003
	s_add_i32 s3, s3, s8
	s_and_b32 s23, s2, 7
	v_lshrrev_b32_e32 v1, 6, v0
	v_and_b32_e32 v2, 63, v0
	s_movk_i32 s11, 0x3000
	v_add_u32_e32 v6, s23, v1
	v_lshlrev_b32_e32 v2, 4, v2
	v_and_b32_e32 v6, 3, v6
	v_and_b32_e32 v5, 31, v0
	v_mad_u32_u24 v6, v6, s11, v2
	v_lshlrev_b32_e32 v5, 2, v5
	s_mul_i32 s9, s23, 11
	s_lshr_b32 s9, s9, 5
	s_mul_i32 s9, s9, 3
	s_sub_i32 s23, s23, s9
	s_add_i32 s9, s23, 1
	s_cmp_ge_u32 s9, 3
	s_cselect_b32 s30, 0, s9
	s_add_i32 s9, s30, 1
	s_cmp_ge_u32 s9, 3
	s_cselect_b32 s31, 0, s9
	s_lshl_b32 s23, s23, 12
	s_lshl_b32 s30, s30, 12
	s_lshl_b32 s31, s31, 12
	s_lshl_b32 s9, s3, 9
	v_add_u32_e32 v2, s23, v6
	v_add_u32_e32 v3, s30, v6
	v_add_u32_e32 v4, s31, v6
	v_add_u32_e32 v5, s9, v5
	s_mul_i32 s8, s10, 0xc000
	s_mul_i32 s9, s3, 0x30000
	s_waitcnt lgkmcnt(0)
	s_load_dword s22, s[14:15], 0x0
	global_load_dword v248, v5, s[12:13]
	global_load_dword v249, v5, s[12:13] offset:128
	global_load_dword v250, v5, s[12:13] offset:256
	global_load_dword v251, v5, s[12:13] offset:384
	s_add_u32 s4, s4, s8
	s_addc_u32 s5, s5, 0
	s_add_u32 s6, s6, s9
	s_addc_u32 s7, s7, 0
	s_add_u32 s16, s6, 0xc000
	s_addc_u32 s17, s7, 0
	s_add_u32 s18, s6, 0x18000
	s_addc_u32 s19, s7, 0
	s_add_u32 s20, s6, 0x24000
	s_addc_u32 s21, s7, 0
	global_load_dwordx4 v[8:11], v2, s[4:5]
	global_load_dwordx4 v[12:15], v2, s[4:5] offset:1024
	global_load_dwordx4 v[56:59], v2, s[6:7]
	global_load_dwordx4 v[104:107], v2, s[16:17]
	global_load_dwordx4 v[152:155], v2, s[18:19]
	global_load_dwordx4 v[200:203], v2, s[20:21]
	global_load_dwordx4 v[16:19], v2, s[4:5] offset:2048
	global_load_dwordx4 v[60:63], v2, s[6:7] offset:1024
	global_load_dwordx4 v[108:111], v2, s[16:17] offset:1024
	global_load_dwordx4 v[156:159], v2, s[18:19] offset:1024
	global_load_dwordx4 v[204:207], v2, s[20:21] offset:1024
	global_load_dwordx4 v[20:23], v2, s[4:5] offset:3072
	global_load_dwordx4 v[64:67], v2, s[6:7] offset:2048
	global_load_dwordx4 v[112:115], v2, s[16:17] offset:2048
	global_load_dwordx4 v[160:163], v2, s[18:19] offset:2048
	global_load_dwordx4 v[208:211], v2, s[20:21] offset:2048
	global_load_dwordx4 v[24:27], v3, s[4:5]
	global_load_dwordx4 v[68:71], v2, s[6:7] offset:3072
	global_load_dwordx4 v[116:119], v2, s[16:17] offset:3072
	global_load_dwordx4 v[164:167], v2, s[18:19] offset:3072
	global_load_dwordx4 v[212:215], v2, s[20:21] offset:3072
	global_load_dwordx4 v[28:31], v3, s[4:5] offset:1024
	global_load_dwordx4 v[72:75], v3, s[6:7]
	global_load_dwordx4 v[120:123], v3, s[16:17]
	global_load_dwordx4 v[168:171], v3, s[18:19]
	global_load_dwordx4 v[216:219], v3, s[20:21]
	global_load_dwordx4 v[32:35], v3, s[4:5] offset:2048
	global_load_dwordx4 v[76:79], v3, s[6:7] offset:1024
	global_load_dwordx4 v[124:127], v3, s[16:17] offset:1024
	global_load_dwordx4 v[172:175], v3, s[18:19] offset:1024
	global_load_dwordx4 v[220:223], v3, s[20:21] offset:1024
	global_load_dwordx4 v[36:39], v3, s[4:5] offset:3072
	global_load_dwordx4 v[80:83], v3, s[6:7] offset:2048
	global_load_dwordx4 v[128:131], v3, s[16:17] offset:2048
	global_load_dwordx4 v[176:179], v3, s[18:19] offset:2048
	global_load_dwordx4 v[224:227], v3, s[20:21] offset:2048
	global_load_dwordx4 v[40:43], v4, s[4:5]
	global_load_dwordx4 v[84:87], v3, s[6:7] offset:3072
	global_load_dwordx4 v[132:135], v3, s[16:17] offset:3072
	global_load_dwordx4 v[180:183], v3, s[18:19] offset:3072
	global_load_dwordx4 v[228:231], v3, s[20:21] offset:3072
	global_load_dwordx4 v[44:47], v4, s[4:5] offset:1024
	global_load_dwordx4 v[88:91], v4, s[6:7]
	global_load_dwordx4 v[136:139], v4, s[16:17]
	global_load_dwordx4 v[184:187], v4, s[18:19]
	global_load_dwordx4 v[232:235], v4, s[20:21]
	global_load_dwordx4 v[48:51], v4, s[4:5] offset:2048
	global_load_dwordx4 v[92:95], v4, s[6:7] offset:1024
	global_load_dwordx4 v[140:143], v4, s[16:17] offset:1024
	global_load_dwordx4 v[188:191], v4, s[18:19] offset:1024
	global_load_dwordx4 v[236:239], v4, s[20:21] offset:1024
	global_load_dwordx4 v[52:55], v4, s[4:5] offset:3072
	global_load_dwordx4 v[96:99], v4, s[6:7] offset:2048
	global_load_dwordx4 v[144:147], v4, s[16:17] offset:2048
	global_load_dwordx4 v[192:195], v4, s[18:19] offset:2048
	global_load_dwordx4 v[240:243], v4, s[20:21] offset:2048
	global_load_dwordx4 v[100:103], v4, s[6:7] offset:3072
	global_load_dwordx4 v[148:151], v4, s[16:17] offset:3072
	global_load_dwordx4 v[196:199], v4, s[18:19] offset:3072
	global_load_dwordx4 v[244:247], v4, s[20:21] offset:3072
	s_waitcnt vmcnt(57)
	v_mfma_f32_32x32x16_bf16 a[0:15], v[8:11], v[56:59], 0
	s_waitcnt vmcnt(56)
	v_mfma_f32_32x32x16_bf16 a[0:15], v[8:11], v[104:107], a[0:15]
	s_waitcnt vmcnt(55)
	v_mfma_f32_32x32x16_bf16 a[0:15], v[8:11], v[152:155], a[0:15]
	s_waitcnt vmcnt(54)
	v_mfma_f32_32x32x16_bf16 a[0:15], v[8:11], v[200:203], a[0:15]
	s_waitcnt vmcnt(52)
	v_mfma_f32_32x32x16_bf16 a[0:15], v[12:15], v[60:63], a[0:15]
	s_waitcnt vmcnt(51)
	v_mfma_f32_32x32x16_bf16 a[0:15], v[12:15], v[108:111], a[0:15]
	s_waitcnt vmcnt(50)
	v_mfma_f32_32x32x16_bf16 a[0:15], v[12:15], v[156:159], a[0:15]
	s_waitcnt vmcnt(49)
	v_mfma_f32_32x32x16_bf16 a[0:15], v[12:15], v[204:207], a[0:15]
	s_waitcnt vmcnt(47)
	v_mfma_f32_32x32x16_bf16 a[0:15], v[16:19], v[64:67], a[0:15]
	s_waitcnt vmcnt(46)
	v_mfma_f32_32x32x16_bf16 a[0:15], v[16:19], v[112:115], a[0:15]
	s_waitcnt vmcnt(45)
	v_mfma_f32_32x32x16_bf16 a[0:15], v[16:19], v[160:163], a[0:15]
	s_waitcnt vmcnt(44)
	v_mfma_f32_32x32x16_bf16 a[0:15], v[16:19], v[208:211], a[0:15]
	s_waitcnt vmcnt(42)
	v_mfma_f32_32x32x16_bf16 a[0:15], v[20:23], v[68:71], a[0:15]
	s_waitcnt vmcnt(41)
	v_mfma_f32_32x32x16_bf16 a[0:15], v[20:23], v[116:119], a[0:15]
	s_waitcnt vmcnt(40)
	v_mfma_f32_32x32x16_bf16 a[0:15], v[20:23], v[164:167], a[0:15]
	s_waitcnt vmcnt(39)
	v_mfma_f32_32x32x16_bf16 a[0:15], v[20:23], v[212:215], a[0:15]
	s_waitcnt vmcnt(37)
	v_mfma_f32_32x32x16_bf16 a[0:15], v[24:27], v[72:75], a[0:15]
	s_waitcnt vmcnt(36)
	v_mfma_f32_32x32x16_bf16 a[0:15], v[24:27], v[120:123], a[0:15]
	s_waitcnt vmcnt(35)
	v_mfma_f32_32x32x16_bf16 a[0:15], v[24:27], v[168:171], a[0:15]
	s_waitcnt vmcnt(34)
	v_mfma_f32_32x32x16_bf16 a[0:15], v[24:27], v[216:219], a[0:15]
	s_waitcnt vmcnt(32)
	v_mfma_f32_32x32x16_bf16 a[0:15], v[28:31], v[76:79], a[0:15]
	s_waitcnt vmcnt(31)
	v_mfma_f32_32x32x16_bf16 a[0:15], v[28:31], v[124:127], a[0:15]
	s_waitcnt vmcnt(30)
	v_mfma_f32_32x32x16_bf16 a[0:15], v[28:31], v[172:175], a[0:15]
	s_waitcnt vmcnt(29)
	v_mfma_f32_32x32x16_bf16 a[0:15], v[28:31], v[220:223], a[0:15]
	s_waitcnt vmcnt(27)
	v_mfma_f32_32x32x16_bf16 a[0:15], v[32:35], v[80:83], a[0:15]
	s_waitcnt vmcnt(26)
	v_mfma_f32_32x32x16_bf16 a[0:15], v[32:35], v[128:131], a[0:15]
	s_waitcnt vmcnt(25)
	v_mfma_f32_32x32x16_bf16 a[0:15], v[32:35], v[176:179], a[0:15]
	s_waitcnt vmcnt(24)
	v_mfma_f32_32x32x16_bf16 a[0:15], v[32:35], v[224:227], a[0:15]
	s_waitcnt vmcnt(22)
	v_mfma_f32_32x32x16_bf16 a[0:15], v[36:39], v[84:87], a[0:15]
	s_waitcnt vmcnt(21)
	v_mfma_f32_32x32x16_bf16 a[0:15], v[36:39], v[132:135], a[0:15]
	s_waitcnt vmcnt(20)
	v_mfma_f32_32x32x16_bf16 a[0:15], v[36:39], v[180:183], a[0:15]
	s_waitcnt vmcnt(19)
	v_mfma_f32_32x32x16_bf16 a[0:15], v[36:39], v[228:231], a[0:15]
	s_waitcnt vmcnt(17)
	v_mfma_f32_32x32x16_bf16 a[0:15], v[40:43], v[88:91], a[0:15]
	s_waitcnt vmcnt(16)
	v_mfma_f32_32x32x16_bf16 a[0:15], v[40:43], v[136:139], a[0:15]
	s_waitcnt vmcnt(15)
	v_mfma_f32_32x32x16_bf16 a[0:15], v[40:43], v[184:187], a[0:15]
	s_waitcnt vmcnt(14)
	v_mfma_f32_32x32x16_bf16 a[0:15], v[40:43], v[232:235], a[0:15]
	s_waitcnt vmcnt(12)
	v_mfma_f32_32x32x16_bf16 a[0:15], v[44:47], v[92:95], a[0:15]
	s_waitcnt vmcnt(11)
	v_mfma_f32_32x32x16_bf16 a[0:15], v[44:47], v[140:143], a[0:15]
	s_waitcnt vmcnt(10)
	v_mfma_f32_32x32x16_bf16 a[0:15], v[44:47], v[188:191], a[0:15]
	s_waitcnt vmcnt(9)
	v_mfma_f32_32x32x16_bf16 a[0:15], v[44:47], v[236:239], a[0:15]
	v_add_f32_e32 v8, 0, v248
	v_add_f32_e32 v8, v8, v249
	v_add_f32_e32 v8, v8, v250
	v_add_f32_e32 v8, v8, v251
	v_mov_b32_e32 v9, 0x3fb8aa3b
	s_waitcnt lgkmcnt(0)
	v_mul_f32_e32 v9, s22, v9
	v_exp_f32_e32 v9, v9
	v_add_f32_e32 v10, 0x2b8cbccc, v8
	v_div_scale_f32 v11, s[8:9], v10, v10, v9
	v_rcp_f32_e32 v12, v11
	v_div_scale_f32 v13, vcc, v9, v10, v9
	v_fma_f32 v14, -v11, v12, 1.0
	v_fmac_f32_e32 v12, v14, v12
	v_mul_f32_e32 v14, v13, v12
	v_fma_f32 v15, -v11, v14, v13
	v_fmac_f32_e32 v14, v15, v12
	v_fma_f32 v11, -v11, v14, v13
	v_div_fmas_f32 v11, v11, v12, v14
	v_div_fixup_f32 v9, v11, v10, v9
	v_lshlrev_b32_e32 v10, 2, v0
	v_add_u32_e32 v10, 0x4000, v10
	v_cmp_gt_u32_e32 vcc, 32, v0
	s_and_saveexec_b64 s[8:9], vcc
	ds_write2_b32 v10, v8, v9 offset0:128 offset1:160
	s_mov_b64 exec, s[8:9]
	s_waitcnt vmcnt(7)
	v_mfma_f32_32x32x16_bf16 a[0:15], v[48:51], v[96:99], a[0:15]
	s_waitcnt vmcnt(6)
	v_mfma_f32_32x32x16_bf16 a[0:15], v[48:51], v[144:147], a[0:15]
	s_waitcnt vmcnt(5)
	v_mfma_f32_32x32x16_bf16 a[0:15], v[48:51], v[192:195], a[0:15]
	s_waitcnt vmcnt(4)
	v_mfma_f32_32x32x16_bf16 a[0:15], v[48:51], v[240:243], a[0:15]
	v_mul_u32_u24_e32 v1, 0x1080, v1
	s_movk_i32 s4, 0x7f
	s_movk_i32 s6, 0x84
	v_cmp_lt_u32_e32 vcc, s4, v0
	v_lshrrev_b32_e32 v11, 3, v0
	v_and_b32_e32 v10, 31, v0
	v_and_b32_e32 v11, 4, v11
	v_mul_u32_u24_e32 v11, 0x84, v11
	v_lshlrev_b32_e32 v9, 2, v10
	v_bfe_u32 v6, v0, 2, 5
	v_and_b32_e32 v7, 3, v0
	v_add3_u32 v1, v1, v11, v9
	v_lshlrev_b32_e32 v8, 3, v7
	s_waitcnt vmcnt(3)
	v_mfma_f32_32x32x16_bf16 a[0:15], v[52:55], v[100:103], a[0:15]
	s_waitcnt vmcnt(2)
	v_mfma_f32_32x32x16_bf16 a[0:15], v[52:55], v[148:151], a[0:15]
	s_waitcnt vmcnt(1)
	v_mfma_f32_32x32x16_bf16 a[0:15], v[52:55], v[196:199], a[0:15]
	s_waitcnt vmcnt(0)
	v_mfma_f32_32x32x16_bf16 a[0:15], v[52:55], v[244:247], a[0:15]
	s_nop 11
	ds_write_b32 v1, a0
	ds_write_b32 v1, a1 offset:132
	ds_write_b32 v1, a2 offset:264
	ds_write_b32 v1, a3 offset:396
	ds_write_b32 v1, a4 offset:1056
	ds_write_b32 v1, a5 offset:1188
	ds_write_b32 v1, a6 offset:1320
	ds_write_b32 v1, a7 offset:1452
	ds_write_b32 v1, a8 offset:2112
	ds_write_b32 v1, a9 offset:2244
	ds_write_b32 v1, a10 offset:2376
	ds_write_b32 v1, a11 offset:2508
	ds_write_b32 v1, a12 offset:3168
	ds_write_b32 v1, a13 offset:3300
	ds_write_b32 v1, a14 offset:3432
	ds_write_b32 v1, a15 offset:3564
	v_bfe_u32 v6, v0, 2, 5
	v_and_b32_e32 v7, 3, v0
	v_lshlrev_b32_e32 v9, 3, v7
	v_readfirstlane_b32 s30, v0
	v_sub_u32_e32 v10, v6, v9
	s_waitcnt lgkmcnt(0)
	s_barrier
	s_cmpk_ge_u32 s30, 0x80
	s_cbranch_scc1 .Llg_k1
	v_mul_u32_u24_e32 v2, 0x84, v6
	v_lshlrev_b32_e32 v8, 5, v7
	v_add_u32_e32 v2, v2, v8
	v_add_u32_e32 v8, 0x4280, v8
	v_add_u32_e32 v3, 0x1080, v2
	v_add_u32_e32 v4, 0x2100, v2
	v_add_u32_e32 v5, 0x3180, v2
	ds_read_b128 v[48:51], v8
	ds_read_b128 v[52:55], v8 offset:16
	ds_read2_b32 v[16:17], v2 offset0:0 offset1:1
	ds_read2_b32 v[18:19], v2 offset0:2 offset1:3
	ds_read2_b32 v[20:21], v2 offset0:4 offset1:5
	ds_read2_b32 v[22:23], v2 offset0:6 offset1:7
	ds_read2_b32 v[24:25], v3 offset0:0 offset1:1
	ds_read2_b32 v[26:27], v3 offset0:2 offset1:3
	ds_read2_b32 v[28:29], v3 offset0:4 offset1:5
	ds_read2_b32 v[30:31], v3 offset0:6 offset1:7
	ds_read2_b32 v[32:33], v4 offset0:0 offset1:1
	ds_read2_b32 v[34:35], v4 offset0:2 offset1:3
	ds_read2_b32 v[36:37], v4 offset0:4 offset1:5
	ds_read2_b32 v[38:39], v4 offset0:6 offset1:7
	s_waitcnt lgkmcnt(4)
	ds_read2_b32 v[40:41], v5 offset0:0 offset1:1
	ds_read2_b32 v[42:43], v5 offset0:2 offset1:3
	ds_read2_b32 v[44:45], v5 offset0:4 offset1:5
	ds_read2_b32 v[46:47], v5 offset0:6 offset1:7
	s_waitcnt lgkmcnt(0)
	s_branch .Llg_join
